# v40 + P2b chunk-top wait counts the Y stores actually issued (vmcnt(count) instead of vmcnt(0)): store acks no longer gate the next chunk
# speedup vs baseline: 1.0120x; 1.0120x over previous
.LBB0_359:
	v_bfe_u32 v171, v165, 4, 2
	s_mul_i32 s13, s12, 3
	v_lshlrev_b32_e32 v173, 10, v171
	v_lshlrev_b32_e32 v169, 7, v169
	s_waitcnt lgkmcnt(0)
	s_barrier
	v_add3_u32 v169, 0, v173, v169
	v_lshlrev_b32_e32 v173, 1, v171
	s_cmp_ge_i32 s13, s37
	v_bfe_u32 v175, v165, 3, 1
	s_cselect_b64 s[44:45], -1, 0
	v_and_or_b32 v173, v173, 2, v175
	s_cmp_lg_u64 s[28:29], 0
	s_mulk_i32 s12, 0x1800
	s_cselect_b64 s[46:47], -1, 0
	v_lshlrev_b32_e32 v173, 5, v173
	s_add_i32 s12, s12, 0
	v_add3_u32 v196, v169, v162, v173
	s_add_i32 s12, s12, 0x10000
	v_lshlrev_b32_e32 v162, 7, v167
	v_lshlrev_b32_e32 v167, 2, v171
	v_and_b32_e32 v197, 7, v165
	v_add3_u32 v198, s12, v162, v167
	v_bitop3_b32 v162, v176, v165, 7 bitop3:0x78
	v_or_b32_e32 v165, 8, v176
	v_or_b32_e32 v167, s20, v165
	v_lshlrev_b32_e32 v184, 7, v165
	v_or_b32_e32 v165, 16, v176
	v_lshl_add_u32 v182, v162, 4, s12
	v_cmp_gt_i32_e64 s[12:13], s36, v167
	v_add_u32_e32 v167, s20, v165
	v_lshlrev_b32_e32 v185, 7, v165
	v_or_b32_e32 v165, 24, v176
	v_cmp_gt_i32_e64 s[14:15], s36, v167
	v_add_u32_e32 v167, s20, v165
	v_lshlrev_b32_e32 v186, 7, v165
	v_or_b32_e32 v165, 32, v176
	v_cmp_gt_i32_e64 s[16:17], s36, v167
	v_add_u32_e32 v167, s20, v165
	v_cmp_gt_i32_e64 s[18:19], s36, v167
	v_lshlrev_b32_e32 v187, 7, v165
	s_waitcnt vmcnt(1)
	v_ashrrev_i32_e32 v167, 31, v166
	v_or_b32_e32 v165, 40, v176
	v_ashrrev_i32_e32 v175, 31, v174
	v_ashrrev_i32_e32 v173, 31, v172
	v_ashrrev_i32_e32 v171, 31, v170
	v_ashrrev_i32_e32 v169, 31, v168
	v_lshlrev_b64 v[180:181], 10, v[166:167]
	v_add_u32_e32 v166, s20, v165
	v_lshlrev_b32_e32 v188, 7, v165
	s_waitcnt vmcnt(0)
	v_ashrrev_i32_e32 v165, 31, v164
	v_lshlrev_b32_e32 v183, 7, v176
	v_lshlrev_b64 v[174:175], 10, v[174:175]
	v_lshlrev_b64 v[172:173], 10, v[172:173]
	v_lshlrev_b64 v[170:171], 10, v[170:171]
	v_lshlrev_b64 v[178:179], 10, v[168:169]
	v_lshlrev_b64 v[176:177], 10, v[164:165]
	v_lshlrev_b32_e32 v162, 4, v197
	v_cmp_gt_i32_e64 s[20:21], s36, v166
	v_lshl_add_u64 v[164:165], s[26:27], 0, v[174:175]
	v_lshl_add_u64 v[166:167], s[26:27], 0, v[172:173]
	v_lshl_add_u64 v[168:169], s[26:27], 0, v[170:171]
	v_lshl_add_u64 v[170:171], s[26:27], 0, v[178:179]
	v_lshl_add_u64 v[172:173], s[26:27], 0, v[180:181]
	v_lshl_add_u64 v[174:175], s[26:27], 0, v[176:177]
	v_lshl_add_u64 v[164:165], v[164:165], 0, v[162:163]
	v_lshl_add_u64 v[166:167], v[166:167], 0, v[162:163]
	v_lshl_add_u64 v[168:169], v[168:169], 0, v[162:163]
	v_lshl_add_u64 v[170:171], v[170:171], 0, v[162:163]
	v_lshl_add_u64 v[172:173], v[172:173], 0, v[162:163]
	v_lshl_add_u64 v[174:175], v[174:175], 0, v[162:163]
	s_mov_b32 s52, 0
	v_add_u32_e32 v162, v182, v183
	v_add_u32_e32 v199, v182, v184
	v_add_u32_e32 v200, v182, v185
	v_add_u32_e32 v201, v182, v186
	v_add_u32_e32 v202, v182, v187
	v_add_u32_e32 v203, v182, v188
	s_mov_b32 s48, 0
	s_mov_b32 s98, 0
	s_branch .LBB0_362

.LBB0_362:
	s_cmp_eq_u32 s98, 6
	s_cbranch_scc0 .Lmy_y6_362
	s_waitcnt vmcnt(6)
	s_branch .Lmy_yd_362
.Lmy_y6_362:
	s_cmp_eq_u32 s98, 5
	s_cbranch_scc0 .Lmy_y5_362
	s_waitcnt vmcnt(5)
	s_branch .Lmy_yd_362
.Lmy_y5_362:
	s_cmp_eq_u32 s98, 4
	s_cbranch_scc0 .Lmy_y4_362
	s_waitcnt vmcnt(4)
	s_branch .Lmy_yd_362
.Lmy_y4_362:
	s_cmp_eq_u32 s98, 3
	s_cbranch_scc0 .Lmy_y3_362
	s_waitcnt vmcnt(3)
	s_branch .Lmy_yd_362
.Lmy_y3_362:
	s_cmp_eq_u32 s98, 2
	s_cbranch_scc0 .Lmy_y2_362
	s_waitcnt vmcnt(2)
	s_branch .Lmy_yd_362
.Lmy_y2_362:
	s_cmp_eq_u32 s98, 1
	s_cbranch_scc0 .Lmy_y1_362
	s_waitcnt vmcnt(1)
	s_branch .Lmy_yd_362

.Lmy_yd_362:
	s_mov_b32 s98, 0
	s_and_b32 s22, s48, 1
	s_lshl_b32 s54, s22, 15
	s_cmp_gt_u32 s48, 13
	s_cselect_b64 s[50:51], -1, 0
	s_and_b64 s[50:51], s[46:47], s[50:51]
	v_sub_co_u32_e64 v176, s[48:49], s48, 14
	s_and_b64 s[56:57], s[46:47], exec
	v_readfirstlane_b32 s53, v176
	s_cselect_b32 s55, s53, 15
	s_add_i32 s53, s53, 16
	s_and_b64 s[48:49], s[48:49], exec
	s_cselect_b32 s48, s53, s55
	s_and_b64 s[50:51], s[50:51], exec
	s_cselect_b32 s55, s29, s43
	s_cselect_b32 s56, s28, s42
	s_mov_b64 s[50:51], -1
	s_andn2_b64 vcc, exec, s[44:45]
	v_subrev_u32_e32 v204, s54, v194
	v_cvt_pk_bf16_f32 v190, v34, v35
	v_cvt_pk_bf16_f32 v191, v36, v37
	v_cvt_pk_bf16_f32 v188, v38, v39
	v_cvt_pk_bf16_f32 v189, v40, v41
	v_cvt_pk_bf16_f32 v186, v42, v43
	v_cvt_pk_bf16_f32 v187, v44, v45
	v_cvt_pk_bf16_f32 v184, v46, v47
	v_cvt_pk_bf16_f32 v185, v48, v49
	v_cvt_pk_bf16_f32 v182, v50, v51
	v_cvt_pk_bf16_f32 v183, v52, v53
	v_cvt_pk_bf16_f32 v180, v54, v55
	v_cvt_pk_bf16_f32 v181, v56, v57
	v_cvt_pk_bf16_f32 v178, v58, v59
	v_cvt_pk_bf16_f32 v179, v60, v61
	v_cvt_pk_bf16_f32 v176, v62, v63
	v_cvt_pk_bf16_f32 v177, v64, v65
	s_cbranch_vccnz .LBB0_364
	s_ashr_i32 s49, s48, 31
	s_lshl_b64 s[50:51], s[48:49], 8
	s_add_u32 s50, s56, s50
	s_addc_u32 s51, s55, s51
	ds_write2st64_b64 v204, v[190:191], v[188:189] offset0:64 offset1:72
	ds_write2st64_b64 v204, v[186:187], v[184:185] offset0:80 offset1:88
	ds_write2st64_b64 v204, v[182:183], v[180:181] offset0:96 offset1:104
	ds_write2st64_b64 v204, v[178:179], v[176:177] offset0:112 offset1:120
	s_add_u32 s58, s50, 0x20000
	global_load_dwordx4 v[34:37], v195, s[50:51]
	s_addc_u32 s59, s51, 0
	global_load_dwordx4 v[38:41], v195, s[58:59]
	s_add_u32 s58, s50, 0x40000
	s_addc_u32 s59, s51, 0
	global_load_dwordx4 v[42:45], v195, s[58:59]
	s_add_u32 s58, s50, 0x60000
	s_addc_u32 s59, s51, 0
	global_load_dwordx4 v[46:49], v195, s[58:59]
	s_add_u32 s58, s50, 0x80000
	s_addc_u32 s59, s51, 0
	global_load_dwordx4 v[50:53], v195, s[58:59]
	s_add_u32 s58, s50, 0xa0000
	s_addc_u32 s59, s51, 0
	global_load_dwordx4 v[54:57], v195, s[58:59]
	s_add_u32 s58, s50, 0xc0000
	s_addc_u32 s59, s51, 0
	global_load_dwordx4 v[58:61], v195, s[58:59]
	s_add_u32 s50, s50, 0xe0000
	s_addc_u32 s51, s51, 0
	global_load_dwordx4 v[62:65], v195, s[50:51]
	s_mov_b64 s[50:51], 0

.LBB0_372:
	ds_read_b128 v[176:179], v162
	v_lshl_add_u64 v[180:181], v[164:165], 0, s[22:23]
	s_waitcnt lgkmcnt(0)
	global_store_dwordx4 v[180:181], v[176:179], off
	s_add_i32 s98, s98, 1
	s_or_b64 exec, exec, s[48:49]
	s_and_saveexec_b64 s[48:49], s[12:13]
	s_cbranch_execz .LBB0_368
.LBB0_373:
	ds_read_b128 v[176:179], v199
	v_lshl_add_u64 v[180:181], v[166:167], 0, s[22:23]
	s_waitcnt lgkmcnt(0)
	global_store_dwordx4 v[180:181], v[176:179], off
	s_add_i32 s98, s98, 1
	s_or_b64 exec, exec, s[48:49]
	s_and_saveexec_b64 s[48:49], s[14:15]
	s_cbranch_execz .LBB0_369
.LBB0_374:
	ds_read_b128 v[176:179], v200
	v_lshl_add_u64 v[180:181], v[168:169], 0, s[22:23]
	s_waitcnt lgkmcnt(0)
	global_store_dwordx4 v[180:181], v[176:179], off
	s_add_i32 s98, s98, 1
	s_or_b64 exec, exec, s[48:49]
	s_and_saveexec_b64 s[48:49], s[16:17]
	s_cbranch_execz .LBB0_370
.LBB0_375:
	ds_read_b128 v[176:179], v201
	v_lshl_add_u64 v[180:181], v[170:171], 0, s[22:23]
	s_waitcnt lgkmcnt(0)
	global_store_dwordx4 v[180:181], v[176:179], off
	s_add_i32 s98, s98, 1
	s_or_b64 exec, exec, s[48:49]
	s_and_saveexec_b64 s[48:49], s[18:19]
	s_cbranch_execz .LBB0_371
.LBB0_376:
	ds_read_b128 v[176:179], v202
	v_lshl_add_u64 v[180:181], v[172:173], 0, s[22:23]
	s_waitcnt lgkmcnt(0)
	global_store_dwordx4 v[180:181], v[176:179], off
	s_add_i32 s98, s98, 1
	s_or_b64 exec, exec, s[48:49]
	s_and_saveexec_b64 s[48:49], s[20:21]
	s_cbranch_execz .LBB0_360
.LBB0_377:
	ds_read_b128 v[176:179], v203
	v_lshl_add_u64 v[180:181], v[174:175], 0, s[22:23]
	s_waitcnt lgkmcnt(0)
	global_store_dwordx4 v[180:181], v[176:179], off
	s_add_i32 s98, s98, 1
	s_branch .LBB0_360

.LBB0_383:
	v_bfe_u32 v139, v131, 4, 2
	s_lshl_b32 s13, s12, 1
	s_waitcnt lgkmcnt(0)
	s_barrier
	v_lshlrev_b32_e32 v140, 10, v139
	v_lshlrev_b32_e32 v137, 7, v137
	s_cmp_ge_i32 s13, s37
	v_add3_u32 v137, 0, v140, v137
	v_lshlrev_b32_e32 v140, 1, v139
	s_cselect_b64 s[20:21], -1, 0
	v_bfe_u32 v141, v131, 3, 1
	v_and_or_b32 v140, v140, 2, v141
	s_cmp_lg_u64 s[28:29], 0
	s_cselect_b64 s[42:43], -1, 0
	s_lshl_b32 s12, s12, 12
	s_add_i32 s12, s12, 0
	v_lshlrev_b32_e32 v140, 5, v140
	s_add_i32 s12, s12, 0x10000
	v_and_b32_e32 v157, 7, v131
	v_bitop3_b32 v131, v138, v131, 7 bitop3:0x78
	v_add3_u32 v156, v137, v135, v140
	v_lshlrev_b32_e32 v133, 7, v133
	v_lshlrev_b32_e32 v135, 2, v139
	v_lshl_add_u32 v142, v131, 4, s12
	v_or_b32_e32 v131, 8, v138
	v_add3_u32 v158, s12, v133, v135
	v_or_b32_e32 v133, s16, v131
	v_lshlrev_b32_e32 v144, 7, v131
	v_or_b32_e32 v131, 16, v138
	v_cmp_gt_i32_e64 s[12:13], s36, v133
	v_or_b32_e32 v133, s16, v131
	v_cmp_gt_i32_e64 s[14:15], s36, v133
	v_lshlrev_b32_e32 v145, 7, v131
	s_waitcnt vmcnt(1)
	v_ashrrev_i32_e32 v133, 31, v132
	v_or_b32_e32 v131, 24, v138
	v_ashrrev_i32_e32 v137, 31, v136
	v_ashrrev_i32_e32 v135, 31, v134
	v_lshlrev_b64 v[140:141], 10, v[132:133]
	v_or_b32_e32 v132, s16, v131
	v_lshlrev_b32_e32 v146, 7, v131
	s_waitcnt vmcnt(0)
	v_ashrrev_i32_e32 v131, 31, v130
	v_lshlrev_b32_e32 v143, 7, v138
	v_lshlrev_b64 v[136:137], 10, v[136:137]
	v_lshlrev_b64 v[134:135], 10, v[134:135]
	v_lshlrev_b64 v[138:139], 10, v[130:131]
	v_lshlrev_b32_e32 v162, 4, v157
	v_cmp_gt_i32_e64 s[16:17], s36, v132
	v_lshl_add_u64 v[130:131], s[26:27], 0, v[136:137]
	v_lshl_add_u64 v[132:133], s[26:27], 0, v[134:135]
	v_lshl_add_u64 v[134:135], s[26:27], 0, v[140:141]
	v_lshl_add_u64 v[136:137], s[26:27], 0, v[138:139]
	v_lshl_add_u64 v[130:131], v[130:131], 0, v[162:163]
	v_lshl_add_u64 v[132:133], v[132:133], 0, v[162:163]
	v_lshl_add_u64 v[134:135], v[134:135], 0, v[162:163]
	v_lshl_add_u64 v[136:137], v[136:137], 0, v[162:163]
	s_mov_b32 s48, 0
	v_add_u32_e32 v159, v142, v143
	v_add_u32_e32 v160, v142, v144
	v_add_u32_e32 v161, v142, v145
	v_add_u32_e32 v162, v142, v146
	s_mov_b32 s44, 0
	s_mov_b32 s98, 0
	s_branch .LBB0_386

.Lmy_yd_386:
	s_mov_b32 s98, 0
	s_and_b32 s22, s44, 1
	s_lshl_b32 s50, s22, 15
	s_cmp_gt_u32 s44, 13
	s_cselect_b64 s[46:47], -1, 0
	s_and_b64 s[46:47], s[42:43], s[46:47]
	v_sub_co_u32_e64 v138, s[44:45], s44, 14
	s_and_b64 s[52:53], s[42:43], exec
	v_readfirstlane_b32 s49, v138
	s_cselect_b32 s51, s49, 15
	s_add_i32 s49, s49, 16
	s_and_b64 s[44:45], s[44:45], exec
	s_cselect_b32 s44, s49, s51
	s_and_b64 s[46:47], s[46:47], exec
	s_cselect_b32 s51, s29, s19
	s_cselect_b32 s52, s28, s18
	s_mov_b64 s[46:47], -1
	s_andn2_b64 vcc, exec, s[20:21]
	v_subrev_u32_e32 v164, s50, v154
	v_cvt_pk_bf16_f32 v152, v34, v35
	v_cvt_pk_bf16_f32 v153, v36, v37
	v_cvt_pk_bf16_f32 v150, v38, v39
	v_cvt_pk_bf16_f32 v151, v40, v41
	v_cvt_pk_bf16_f32 v148, v42, v43
	v_cvt_pk_bf16_f32 v149, v44, v45
	v_cvt_pk_bf16_f32 v146, v46, v47
	v_cvt_pk_bf16_f32 v147, v48, v49
	v_cvt_pk_bf16_f32 v144, v50, v51
	v_cvt_pk_bf16_f32 v145, v52, v53
	v_cvt_pk_bf16_f32 v142, v54, v55
	v_cvt_pk_bf16_f32 v143, v56, v57
	v_cvt_pk_bf16_f32 v140, v58, v59
	v_cvt_pk_bf16_f32 v141, v60, v61
	v_cvt_pk_bf16_f32 v138, v62, v63
	v_cvt_pk_bf16_f32 v139, v64, v65
	s_cbranch_vccnz .LBB0_388
	s_ashr_i32 s45, s44, 31
	s_lshl_b64 s[46:47], s[44:45], 8
	s_add_u32 s46, s52, s46
	s_addc_u32 s47, s51, s47
	ds_write2st64_b64 v164, v[152:153], v[150:151] offset0:64 offset1:72
	ds_write2st64_b64 v164, v[148:149], v[146:147] offset0:80 offset1:88
	ds_write2st64_b64 v164, v[144:145], v[142:143] offset0:96 offset1:104
	ds_write2st64_b64 v164, v[140:141], v[138:139] offset0:112 offset1:120
	s_add_u32 s54, s46, 0x20000
	global_load_dwordx4 v[34:37], v155, s[46:47]
	s_addc_u32 s55, s47, 0
	global_load_dwordx4 v[38:41], v155, s[54:55]
	s_add_u32 s54, s46, 0x40000
	s_addc_u32 s55, s47, 0
	global_load_dwordx4 v[42:45], v155, s[54:55]
	s_add_u32 s54, s46, 0x60000
	s_addc_u32 s55, s47, 0
	global_load_dwordx4 v[46:49], v155, s[54:55]
	s_add_u32 s54, s46, 0x80000
	s_addc_u32 s55, s47, 0
	global_load_dwordx4 v[50:53], v155, s[54:55]
	s_add_u32 s54, s46, 0xa0000
	s_addc_u32 s55, s47, 0
	global_load_dwordx4 v[54:57], v155, s[54:55]
	s_add_u32 s54, s46, 0xc0000
	s_addc_u32 s55, s47, 0
	global_load_dwordx4 v[58:61], v155, s[54:55]
	s_add_u32 s46, s46, 0xe0000
	s_addc_u32 s47, s47, 0
	global_load_dwordx4 v[62:65], v155, s[46:47]
	s_mov_b64 s[46:47], 0

.LBB0_394:
	ds_read_b128 v[138:141], v159
	v_lshl_add_u64 v[142:143], v[130:131], 0, s[22:23]
	s_waitcnt lgkmcnt(0)
	global_store_dwordx4 v[142:143], v[138:141], off
	s_add_i32 s98, s98, 1
	s_or_b64 exec, exec, s[44:45]
	s_and_saveexec_b64 s[44:45], s[12:13]
	s_cbranch_execz .LBB0_392
.LBB0_395:
	ds_read_b128 v[138:141], v160
	v_lshl_add_u64 v[142:143], v[132:133], 0, s[22:23]
	s_waitcnt lgkmcnt(0)
	global_store_dwordx4 v[142:143], v[138:141], off
	s_add_i32 s98, s98, 1
	s_or_b64 exec, exec, s[44:45]
	s_and_saveexec_b64 s[44:45], s[14:15]
	s_cbranch_execz .LBB0_393
.LBB0_396:
	ds_read_b128 v[138:141], v161
	v_lshl_add_u64 v[142:143], v[134:135], 0, s[22:23]
	s_waitcnt lgkmcnt(0)
	global_store_dwordx4 v[142:143], v[138:141], off
	s_add_i32 s98, s98, 1
	s_or_b64 exec, exec, s[44:45]
	s_and_saveexec_b64 s[44:45], s[16:17]
	s_cbranch_execz .LBB0_384
.LBB0_397:
	ds_read_b128 v[138:141], v162
	v_lshl_add_u64 v[142:143], v[136:137], 0, s[22:23]
	s_waitcnt lgkmcnt(0)
	global_store_dwordx4 v[142:143], v[138:141], off
	s_add_i32 s98, s98, 1
	s_branch .LBB0_384

.LBB0_403:
	v_bfe_u32 v73, v67, 4, 2
	s_waitcnt lgkmcnt(0)
	s_barrier
	v_lshlrev_b32_e32 v74, 10, v73
	v_lshlrev_b32_e32 v72, 7, v72
	s_cmp_ge_i32 s13, s37
	v_add3_u32 v72, 0, v74, v72
	v_lshlrev_b32_e32 v74, 1, v73
	s_cselect_b64 s[16:17], -1, 0
	v_bfe_u32 v75, v67, 3, 1
	v_and_or_b32 v74, v74, 2, v75
	s_cmp_lg_u64 s[28:29], 0
	s_cselect_b64 s[18:19], -1, 0
	s_lshl_b32 s13, s13, 11
	s_add_i32 s13, s13, 0
	v_lshlrev_b32_e32 v74, 5, v74
	s_add_i32 s13, s13, 0x10000
	v_and_b32_e32 v89, 7, v67
	v_bitop3_b32 v67, v70, v67, 7 bitop3:0x78
	v_add3_u32 v88, v72, v71, v74
	v_lshlrev_b32_e32 v69, 7, v69
	v_lshlrev_b32_e32 v71, 2, v73
	v_lshl_add_u32 v72, v67, 4, s13
	v_or_b32_e32 v67, 8, v70
	v_add3_u32 v90, s13, v69, v71
	v_lshlrev_b32_e32 v73, 7, v70
	s_waitcnt vmcnt(1)
	v_ashrrev_i32_e32 v69, 31, v68
	v_or_b32_e32 v70, s12, v67
	v_lshlrev_b32_e32 v74, 7, v67
	s_waitcnt vmcnt(0)
	v_ashrrev_i32_e32 v67, 31, v66
	v_lshlrev_b64 v[68:69], 10, v[68:69]
	v_cmp_gt_i32_e64 s[12:13], s36, v70
	v_lshlrev_b64 v[70:71], 10, v[66:67]
	v_lshlrev_b32_e32 v162, 4, v89
	v_lshl_add_u64 v[66:67], s[26:27], 0, v[68:69]
	v_lshl_add_u64 v[68:69], s[26:27], 0, v[70:71]
	v_lshl_add_u64 v[66:67], v[66:67], 0, v[162:163]
	v_lshl_add_u64 v[68:69], v[68:69], 0, v[162:163]
	s_mov_b32 s34, 0
	v_add_u32_e32 v91, v72, v73
	v_add_u32_e32 v92, v72, v74
	s_mov_b32 s20, 0
	s_mov_b32 s98, 0
	s_branch .LBB0_406

.Lmy_yd_406:
	s_mov_b32 s98, 0
	s_and_b32 s22, s20, 1
	s_lshl_b32 s36, s22, 15
	s_cmp_gt_u32 s20, 13
	s_cselect_b64 s[30:31], -1, 0
	s_and_b64 s[30:31], s[18:19], s[30:31]
	v_sub_co_u32_e64 v70, s[20:21], s20, 14
	s_and_b64 s[38:39], s[18:19], exec
	v_readfirstlane_b32 s35, v70
	s_cselect_b32 s37, s35, 15
	s_add_i32 s35, s35, 16
	s_and_b64 s[20:21], s[20:21], exec
	s_cselect_b32 s20, s35, s37
	s_and_b64 s[30:31], s[30:31], exec
	s_cselect_b32 s37, s29, s15
	s_cselect_b32 s38, s28, s14
	s_mov_b64 s[30:31], -1
	s_andn2_b64 vcc, exec, s[16:17]
	v_subrev_u32_e32 v93, s36, v86
	v_cvt_pk_bf16_f32 v84, v2, v3
	v_cvt_pk_bf16_f32 v85, v4, v5
	v_cvt_pk_bf16_f32 v82, v6, v7
	v_cvt_pk_bf16_f32 v83, v8, v9
	v_cvt_pk_bf16_f32 v80, v10, v11
	v_cvt_pk_bf16_f32 v81, v12, v13
	v_cvt_pk_bf16_f32 v78, v14, v15
	v_cvt_pk_bf16_f32 v79, v16, v17
	v_cvt_pk_bf16_f32 v76, v18, v19
	v_cvt_pk_bf16_f32 v77, v20, v21
	v_cvt_pk_bf16_f32 v74, v22, v23
	v_cvt_pk_bf16_f32 v75, v24, v25
	v_cvt_pk_bf16_f32 v72, v26, v27
	v_cvt_pk_bf16_f32 v73, v28, v29
	v_cvt_pk_bf16_f32 v70, v30, v31
	v_cvt_pk_bf16_f32 v71, v32, v33
	s_cbranch_vccnz .LBB0_408
	s_ashr_i32 s21, s20, 31
	s_lshl_b64 s[30:31], s[20:21], 8
	s_add_u32 s30, s38, s30
	s_addc_u32 s31, s37, s31
	ds_write2st64_b64 v93, v[84:85], v[82:83] offset0:64 offset1:72
	ds_write2st64_b64 v93, v[80:81], v[78:79] offset0:80 offset1:88
	ds_write2st64_b64 v93, v[76:77], v[74:75] offset0:96 offset1:104
	ds_write2st64_b64 v93, v[72:73], v[70:71] offset0:112 offset1:120
	s_add_u32 s40, s30, 0x20000
	global_load_dwordx4 v[2:5], v87, s[30:31]
	s_addc_u32 s41, s31, 0
	global_load_dwordx4 v[6:9], v87, s[40:41]
	s_add_u32 s40, s30, 0x40000
	s_addc_u32 s41, s31, 0
	global_load_dwordx4 v[10:13], v87, s[40:41]
	s_add_u32 s40, s30, 0x60000
	s_addc_u32 s41, s31, 0
	global_load_dwordx4 v[14:17], v87, s[40:41]
	s_add_u32 s40, s30, 0x80000
	s_addc_u32 s41, s31, 0
	global_load_dwordx4 v[18:21], v87, s[40:41]
	s_add_u32 s40, s30, 0xa0000
	s_addc_u32 s41, s31, 0
	global_load_dwordx4 v[22:25], v87, s[40:41]
	s_add_u32 s40, s30, 0xc0000
	s_addc_u32 s41, s31, 0
	global_load_dwordx4 v[26:29], v87, s[40:41]
	s_add_u32 s30, s30, 0xe0000
	s_addc_u32 s31, s31, 0
	global_load_dwordx4 v[30:33], v87, s[30:31]
	s_mov_b64 s[30:31], 0
.LBB0_408:
	s_andn2_b64 vcc, exec, s[30:31]
	s_cbranch_vccnz .LBB0_405
	v_mov_b32_e32 v14, v88
	s_ashr_i32 s21, s20, 31
	v_add_u32_e32 v106, s36, v14
	ds_read_b64_tr_b16 v[2:3], v106
	ds_read_b64_tr_b16 v[4:5], v106 offset:512
	v_xad_u32 v107, v14, 32, s36
	v_xad_u32 v108, v14, 64, s36
	ds_read_b64_tr_b16 v[6:7], v107
	ds_read_b64_tr_b16 v[8:9], v107 offset:512
	ds_read_b64_tr_b16 v[10:11], v108
	ds_read_b64_tr_b16 v[12:13], v108 offset:512
	s_waitcnt lgkmcnt(4)
	v_mfma_f32_16x16x32_bf16 v[2:5], v[2:5], v[34:37], 0
	s_lshl_b64 s[20:21], s[20:21], 8
	s_add_u32 s20, s38, s20
	s_addc_u32 s21, s37, s21
	ds_write_b64 v93, v[84:85] offset:32768
	v_xor_b32_e32 v14, 0x60, v14
	v_add_u32_e32 v109, s36, v14
	ds_read_b64_tr_b16 v[14:15], v109
	ds_read_b64_tr_b16 v[16:17], v109 offset:512
	s_waitcnt lgkmcnt(5)
	v_mfma_f32_16x16x32_bf16 v[6:9], v[6:9], v[34:37], 0
	ds_write_b64 v93, v[82:83] offset:36864
	ds_read_b64_tr_b16 v[18:19], v106 offset:4096
	ds_read_b64_tr_b16 v[20:21], v106 offset:4608
	s_waitcnt lgkmcnt(6)
	v_mfma_f32_16x16x32_bf16 v[10:13], v[10:13], v[34:37], 0
	ds_write_b64 v93, v[80:81] offset:40960
	ds_read_b64_tr_b16 v[22:23], v107 offset:4096
	ds_read_b64_tr_b16 v[24:25], v107 offset:4608
	s_waitcnt lgkmcnt(6)
	v_mfma_f32_16x16x32_bf16 v[14:17], v[14:17], v[34:37], 0
	ds_write_b64 v93, v[78:79] offset:45056
	ds_read_b64_tr_b16 v[26:27], v108 offset:4096
	ds_read_b64_tr_b16 v[28:29], v108 offset:4608
	s_waitcnt lgkmcnt(6)
	v_mfma_f32_16x16x32_bf16 v[2:5], v[18:21], v[38:41], v[2:5]
	ds_write_b64 v93, v[76:77] offset:49152
	ds_read_b64_tr_b16 v[18:19], v109 offset:4096
	ds_read_b64_tr_b16 v[20:21], v109 offset:4608
	s_waitcnt lgkmcnt(6)
	v_mfma_f32_16x16x32_bf16 v[6:9], v[22:25], v[38:41], v[6:9]
	ds_write_b64 v93, v[74:75] offset:53248
	ds_read_b64_tr_b16 v[22:23], v106 offset:8192
	ds_read_b64_tr_b16 v[24:25], v106 offset:8704
	s_waitcnt lgkmcnt(6)
	v_mfma_f32_16x16x32_bf16 v[10:13], v[26:29], v[38:41], v[10:13]
	ds_write_b64 v93, v[72:73] offset:57344
	ds_read_b64_tr_b16 v[26:27], v107 offset:8192
	ds_read_b64_tr_b16 v[28:29], v107 offset:8704
	s_waitcnt lgkmcnt(6)
	v_mfma_f32_16x16x32_bf16 v[14:17], v[18:21], v[38:41], v[14:17]
	ds_write_b64 v93, v[70:71] offset:61440
	ds_read_b64_tr_b16 v[18:19], v108 offset:8192
	ds_read_b64_tr_b16 v[20:21], v108 offset:8704
	s_waitcnt lgkmcnt(6)
	v_mfma_f32_16x16x32_bf16 v[22:25], v[22:25], v[42:45], v[2:5]
	global_load_dwordx4 v[2:5], v87, s[20:21]
	ds_read_b64_tr_b16 v[30:31], v109 offset:8192
	ds_read_b64_tr_b16 v[32:33], v109 offset:8704
	s_waitcnt lgkmcnt(5)
	v_mfma_f32_16x16x32_bf16 v[26:29], v[26:29], v[42:45], v[6:9]
	s_add_u32 s30, s20, 0x20000
	s_addc_u32 s31, s21, 0
	global_load_dwordx4 v[6:9], v87, s[30:31]
	ds_read_b64_tr_b16 v[70:71], v106 offset:12288
	ds_read_b64_tr_b16 v[72:73], v106 offset:12800
	s_add_u32 s30, s20, 0x40000
	s_waitcnt lgkmcnt(4)
	v_mfma_f32_16x16x32_bf16 v[74:77], v[18:21], v[42:45], v[10:13]
	s_addc_u32 s31, s21, 0
	global_load_dwordx4 v[10:13], v87, s[30:31]
	ds_read_b64_tr_b16 v[78:79], v107 offset:12288
	ds_read_b64_tr_b16 v[80:81], v107 offset:12800
	s_waitcnt lgkmcnt(4)
	v_mfma_f32_16x16x32_bf16 v[30:33], v[30:33], v[42:45], v[14:17]
	s_add_u32 s30, s20, 0x60000
	s_addc_u32 s31, s21, 0
	global_load_dwordx4 v[14:17], v87, s[30:31]
	ds_read_b64_tr_b16 v[82:83], v108 offset:12288
	ds_read_b64_tr_b16 v[84:85], v108 offset:12800
	s_add_u32 s30, s20, 0x80000
	s_addc_u32 s31, s21, 0
	global_load_dwordx4 v[18:21], v87, s[30:31]
	s_waitcnt lgkmcnt(4)
	v_mfma_f32_16x16x32_bf16 v[70:73], v[70:73], v[46:49], v[22:25]
	ds_read_b64_tr_b16 v[94:95], v109 offset:12288
	ds_read_b64_tr_b16 v[96:97], v109 offset:12800
	s_add_u32 s30, s20, 0xa0000
	s_addc_u32 s31, s21, 0
	global_load_dwordx4 v[22:25], v87, s[30:31]
	s_waitcnt lgkmcnt(4)
	v_mfma_f32_16x16x32_bf16 v[78:81], v[78:81], v[46:49], v[26:29]
	ds_read_b64_tr_b16 v[98:99], v106 offset:16384
	ds_read_b64_tr_b16 v[100:101], v106 offset:16896
	s_add_u32 s30, s20, 0xc0000
	s_addc_u32 s31, s21, 0
	global_load_dwordx4 v[26:29], v87, s[30:31]
	s_waitcnt lgkmcnt(4)
	v_mfma_f32_16x16x32_bf16 v[74:77], v[82:85], v[46:49], v[74:77]
	ds_read_b64_tr_b16 v[82:83], v107 offset:16384
	ds_read_b64_tr_b16 v[84:85], v107 offset:16896
	s_add_u32 s20, s20, 0xe0000
	s_waitcnt lgkmcnt(4)
	v_mfma_f32_16x16x32_bf16 v[94:97], v[94:97], v[46:49], v[30:33]
	s_addc_u32 s21, s21, 0
	global_load_dwordx4 v[30:33], v87, s[20:21]
	ds_read_b64_tr_b16 v[102:103], v108 offset:16384
	ds_read_b64_tr_b16 v[104:105], v108 offset:16896
	s_waitcnt lgkmcnt(4)
	v_mfma_f32_16x16x32_bf16 v[70:73], v[98:101], v[50:53], v[70:73]
	ds_read_b64_tr_b16 v[98:99], v109 offset:16384
	ds_read_b64_tr_b16 v[100:101], v109 offset:16896
	s_waitcnt lgkmcnt(4)
	v_mfma_f32_16x16x32_bf16 v[78:81], v[82:85], v[50:53], v[78:81]
	ds_read_b64_tr_b16 v[82:83], v106 offset:20480
	ds_read_b64_tr_b16 v[84:85], v106 offset:20992
	s_waitcnt lgkmcnt(4)
	v_mfma_f32_16x16x32_bf16 v[74:77], v[102:105], v[50:53], v[74:77]
	ds_read_b64_tr_b16 v[102:103], v107 offset:20480
	ds_read_b64_tr_b16 v[104:105], v107 offset:20992
	s_waitcnt lgkmcnt(4)
	v_mfma_f32_16x16x32_bf16 v[94:97], v[98:101], v[50:53], v[94:97]
	ds_read_b64_tr_b16 v[98:99], v108 offset:20480
	ds_read_b64_tr_b16 v[100:101], v108 offset:20992
	s_waitcnt lgkmcnt(4)
	v_mfma_f32_16x16x32_bf16 v[70:73], v[82:85], v[54:57], v[70:73]
	ds_read_b64_tr_b16 v[82:83], v109 offset:20480
	ds_read_b64_tr_b16 v[84:85], v109 offset:20992
	s_waitcnt lgkmcnt(4)
	v_mfma_f32_16x16x32_bf16 v[78:81], v[102:105], v[54:57], v[78:81]
	ds_read_b64_tr_b16 v[102:103], v106 offset:24576
	ds_read_b64_tr_b16 v[104:105], v106 offset:25088
	s_waitcnt lgkmcnt(4)
	v_mfma_f32_16x16x32_bf16 v[74:77], v[98:101], v[54:57], v[74:77]
	ds_read_b64_tr_b16 v[98:99], v107 offset:24576
	ds_read_b64_tr_b16 v[100:101], v107 offset:25088
	s_waitcnt lgkmcnt(4)
	v_mfma_f32_16x16x32_bf16 v[82:85], v[82:85], v[54:57], v[94:97]
	s_nop 2
	ds_read_b64_tr_b16 v[94:95], v108 offset:24576
	ds_read_b64_tr_b16 v[96:97], v108 offset:25088
	s_waitcnt lgkmcnt(4)
	v_mfma_f32_16x16x32_bf16 v[70:73], v[102:105], v[58:61], v[70:73]
	ds_read_b64_tr_b16 v[102:103], v109 offset:24576
	ds_read_b64_tr_b16 v[104:105], v109 offset:25088
	s_waitcnt lgkmcnt(4)
	v_mfma_f32_16x16x32_bf16 v[78:81], v[98:101], v[58:61], v[78:81]
	ds_read_b64_tr_b16 v[98:99], v106 offset:28672
	ds_read_b64_tr_b16 v[100:101], v106 offset:29184
	s_waitcnt lgkmcnt(4)
	v_mfma_f32_16x16x32_bf16 v[74:77], v[94:97], v[58:61], v[74:77]
	ds_read_b64_tr_b16 v[94:95], v107 offset:28672
	ds_read_b64_tr_b16 v[96:97], v107 offset:29184
	s_waitcnt lgkmcnt(4)
	v_mfma_f32_16x16x32_bf16 v[82:85], v[102:105], v[58:61], v[82:85]
	ds_read_b64_tr_b16 v[102:103], v108 offset:28672
	ds_read_b64_tr_b16 v[104:105], v108 offset:29184
	s_waitcnt lgkmcnt(4)
	v_mfma_f32_16x16x32_bf16 v[70:73], v[98:101], v[62:65], v[70:73]
	ds_read_b64_tr_b16 v[98:99], v109 offset:28672
	ds_read_b64_tr_b16 v[100:101], v109 offset:29184
	s_waitcnt lgkmcnt(4)
	v_mfma_f32_16x16x32_bf16 v[78:81], v[94:97], v[62:65], v[78:81]
	s_waitcnt lgkmcnt(2)
	v_mfma_f32_16x16x32_bf16 v[74:77], v[102:105], v[62:65], v[74:77]
	s_waitcnt lgkmcnt(0)
	v_mfma_f32_16x16x32_bf16 v[82:85], v[98:101], v[62:65], v[82:85]
	v_mul_f32_e32 v70, 0x41800000, v70
	v_mul_f32_e32 v71, 0x41800000, v71
	v_mov_b32_e32 v93, 0
	v_cvt_pk_fp8_f32 v93, v70, v71
	v_mul_f32_e32 v70, 0x41800000, v72
	v_mul_f32_e32 v71, 0x41800000, v73
	v_mul_f32_e32 v72, 0x41800000, v79
	v_cvt_pk_fp8_f32 v93, v70, v71 op_sel:[0,0,1]
	v_mul_f32_e32 v71, 0x41800000, v78
	v_mov_b32_e32 v73, 0
	s_lshl_b32 s20, s22, 2
	v_cvt_pk_fp8_f32 v73, v71, v72
	v_xor_b32_e32 v70, s20, v89
	v_lshl_add_u32 v70, v70, 4, v90
	ds_write_b32 v70, v93
	v_mul_f32_e32 v70, 0x41800000, v80
	v_mul_f32_e32 v71, 0x41800000, v81
	v_cvt_pk_fp8_f32 v73, v70, v71 op_sel:[0,0,1]
	v_mul_f32_e32 v71, 0x41800000, v74
	v_mul_f32_e32 v72, 0x41800000, v75
	v_mov_b32_e32 v74, 0
	v_cvt_pk_fp8_f32 v74, v71, v72
	v_bitop3_b32 v70, s20, v89, 1 bitop3:0x36
	v_lshl_add_u32 v70, v70, 4, v90
	ds_write_b32 v70, v73
	v_mul_f32_e32 v70, 0x41800000, v76
	v_mul_f32_e32 v71, 0x41800000, v77
	v_cvt_pk_fp8_f32 v74, v70, v71 op_sel:[0,0,1]
	v_mul_f32_e32 v71, 0x41800000, v82
	v_mul_f32_e32 v72, 0x41800000, v83
	v_mov_b32_e32 v73, 0
	v_cvt_pk_fp8_f32 v73, v71, v72
	v_bitop3_b32 v70, s20, v89, 2 bitop3:0x36
	v_lshl_add_u32 v70, v70, 4, v90
	ds_write_b32 v70, v74
	v_mul_f32_e32 v70, 0x41800000, v84
	v_mul_f32_e32 v71, 0x41800000, v85
	v_cvt_pk_fp8_f32 v73, v70, v71 op_sel:[0,0,1]
	v_bitop3_b32 v70, s20, v89, 3 bitop3:0x36
	v_lshl_add_u32 v70, v70, 4, v90
	s_cmp_eq_u32 s22, 0
	ds_write_b32 v70, v73
	s_cbranch_scc1 .LBB0_405
	s_waitcnt lgkmcnt(0)
	s_and_b32 s22, s34, 0x380
	s_and_saveexec_b64 s[20:21], s[10:11]
	s_cbranch_execz .LBB0_412
	ds_read_b128 v[70:73], v91
	v_lshl_add_u64 v[74:75], v[66:67], 0, s[22:23]
	s_waitcnt lgkmcnt(0)
	global_store_dwordx4 v[74:75], v[70:73], off
	s_add_i32 s98, s98, 1
.LBB0_412:
	s_or_b64 exec, exec, s[20:21]
	s_and_saveexec_b64 s[20:21], s[12:13]
	s_cbranch_execz .LBB0_404
	ds_read_b128 v[70:73], v92
	v_lshl_add_u64 v[74:75], v[68:69], 0, s[22:23]
	s_waitcnt lgkmcnt(0)
	global_store_dwordx4 v[74:75], v[70:73], off
	s_add_i32 s98, s98, 1
	s_branch .LBB0_404

.LBB0_965:
	v_bfe_u32 v171, v165, 4, 2
	s_mul_i32 s13, s12, 3
	v_lshlrev_b32_e32 v173, 10, v171
	v_lshlrev_b32_e32 v169, 7, v169
	s_waitcnt lgkmcnt(0)
	s_barrier
	v_add3_u32 v169, 0, v173, v169
	v_lshlrev_b32_e32 v173, 1, v171
	s_cmp_ge_i32 s13, s49
	v_bfe_u32 v175, v165, 3, 1
	s_cselect_b64 s[40:41], -1, 0
	v_and_or_b32 v173, v173, 2, v175
	s_cmp_lg_u64 s[28:29], 0
	s_mulk_i32 s12, 0x1800
	s_cselect_b64 s[42:43], -1, 0
	v_lshlrev_b32_e32 v173, 5, v173
	s_add_i32 s12, s12, 0
	v_add3_u32 v196, v169, v162, v173
	s_add_i32 s12, s12, 0x10000
	v_lshlrev_b32_e32 v162, 7, v167
	v_lshlrev_b32_e32 v167, 2, v171
	v_and_b32_e32 v197, 7, v165
	v_add3_u32 v198, s12, v162, v167
	v_bitop3_b32 v162, v176, v165, 7 bitop3:0x78
	v_or_b32_e32 v165, 8, v176
	v_or_b32_e32 v167, s20, v165
	v_lshlrev_b32_e32 v184, 7, v165
	v_or_b32_e32 v165, 16, v176
	v_lshl_add_u32 v182, v162, 4, s12
	v_cmp_gt_i32_e64 s[12:13], s48, v167
	v_add_u32_e32 v167, s20, v165
	v_lshlrev_b32_e32 v185, 7, v165
	v_or_b32_e32 v165, 24, v176
	v_cmp_gt_i32_e64 s[14:15], s48, v167
	v_add_u32_e32 v167, s20, v165
	v_lshlrev_b32_e32 v186, 7, v165
	v_or_b32_e32 v165, 32, v176
	v_cmp_gt_i32_e64 s[16:17], s48, v167
	v_add_u32_e32 v167, s20, v165
	v_cmp_gt_i32_e64 s[18:19], s48, v167
	v_lshlrev_b32_e32 v187, 7, v165
	s_waitcnt vmcnt(1)
	v_ashrrev_i32_e32 v167, 31, v166
	v_or_b32_e32 v165, 40, v176
	v_ashrrev_i32_e32 v175, 31, v174
	v_ashrrev_i32_e32 v173, 31, v172
	v_ashrrev_i32_e32 v171, 31, v170
	v_ashrrev_i32_e32 v169, 31, v168
	v_lshlrev_b64 v[180:181], 10, v[166:167]
	v_add_u32_e32 v166, s20, v165
	v_lshlrev_b32_e32 v188, 7, v165
	s_waitcnt vmcnt(0)
	v_ashrrev_i32_e32 v165, 31, v164
	v_lshlrev_b32_e32 v183, 7, v176
	v_lshlrev_b64 v[174:175], 10, v[174:175]
	v_lshlrev_b64 v[172:173], 10, v[172:173]
	v_lshlrev_b64 v[170:171], 10, v[170:171]
	v_lshlrev_b64 v[178:179], 10, v[168:169]
	v_lshlrev_b64 v[176:177], 10, v[164:165]
	v_lshlrev_b32_e32 v162, 4, v197
	v_cmp_gt_i32_e64 s[20:21], s48, v166
	v_lshl_add_u64 v[164:165], s[26:27], 0, v[174:175]
	v_lshl_add_u64 v[166:167], s[26:27], 0, v[172:173]
	v_lshl_add_u64 v[168:169], s[26:27], 0, v[170:171]
	v_lshl_add_u64 v[170:171], s[26:27], 0, v[178:179]
	v_lshl_add_u64 v[172:173], s[26:27], 0, v[180:181]
	v_lshl_add_u64 v[174:175], s[26:27], 0, v[176:177]
	v_lshl_add_u64 v[164:165], v[164:165], 0, v[162:163]
	v_lshl_add_u64 v[166:167], v[166:167], 0, v[162:163]
	v_lshl_add_u64 v[168:169], v[168:169], 0, v[162:163]
	v_lshl_add_u64 v[170:171], v[170:171], 0, v[162:163]
	v_lshl_add_u64 v[172:173], v[172:173], 0, v[162:163]
	v_lshl_add_u64 v[174:175], v[174:175], 0, v[162:163]
	s_mov_b32 s52, 0
	v_add_u32_e32 v162, v182, v183
	v_add_u32_e32 v199, v182, v184
	v_add_u32_e32 v200, v182, v185
	v_add_u32_e32 v201, v182, v186
	v_add_u32_e32 v202, v182, v187
	v_add_u32_e32 v203, v182, v188
	s_mov_b32 s44, 0
	s_mov_b32 s98, 0
	s_branch .LBB0_968

.Lmy_yd_968:
	s_mov_b32 s98, 0
	s_and_b32 s22, s44, 1
	s_lshl_b32 s54, s22, 15
	s_cmp_gt_u32 s44, 13
	s_cselect_b64 s[46:47], -1, 0
	s_and_b64 s[46:47], s[42:43], s[46:47]
	v_sub_co_u32_e64 v176, s[44:45], s44, 14
	s_and_b64 s[56:57], s[42:43], exec
	v_readfirstlane_b32 s53, v176
	s_cselect_b32 s55, s53, 15
	s_add_i32 s53, s53, 16
	s_and_b64 s[44:45], s[44:45], exec
	s_cselect_b32 s44, s53, s55
	s_and_b64 s[46:47], s[46:47], exec
	s_cselect_b32 s55, s29, s39
	s_cselect_b32 s56, s28, s38
	s_mov_b64 s[46:47], -1
	s_andn2_b64 vcc, exec, s[40:41]
	v_subrev_u32_e32 v204, s54, v194
	v_cvt_pk_bf16_f32 v190, v34, v35
	v_cvt_pk_bf16_f32 v191, v36, v37
	v_cvt_pk_bf16_f32 v188, v38, v39
	v_cvt_pk_bf16_f32 v189, v40, v41
	v_cvt_pk_bf16_f32 v186, v42, v43
	v_cvt_pk_bf16_f32 v187, v44, v45
	v_cvt_pk_bf16_f32 v184, v46, v47
	v_cvt_pk_bf16_f32 v185, v48, v49
	v_cvt_pk_bf16_f32 v182, v50, v51
	v_cvt_pk_bf16_f32 v183, v52, v53
	v_cvt_pk_bf16_f32 v180, v54, v55
	v_cvt_pk_bf16_f32 v181, v56, v57
	v_cvt_pk_bf16_f32 v178, v58, v59
	v_cvt_pk_bf16_f32 v179, v60, v61
	v_cvt_pk_bf16_f32 v176, v62, v63
	v_cvt_pk_bf16_f32 v177, v64, v65
	s_cbranch_vccnz .LBB0_970
	s_ashr_i32 s45, s44, 31
	s_lshl_b64 s[46:47], s[44:45], 8
	s_add_u32 s46, s56, s46
	s_addc_u32 s47, s55, s47
	ds_write2st64_b64 v204, v[190:191], v[188:189] offset0:64 offset1:72
	ds_write2st64_b64 v204, v[186:187], v[184:185] offset0:80 offset1:88
	ds_write2st64_b64 v204, v[182:183], v[180:181] offset0:96 offset1:104
	ds_write2st64_b64 v204, v[178:179], v[176:177] offset0:112 offset1:120
	s_add_u32 s58, s46, 0x20000
	global_load_dwordx4 v[34:37], v195, s[46:47]
	s_addc_u32 s59, s47, 0
	global_load_dwordx4 v[38:41], v195, s[58:59]
	s_add_u32 s58, s46, 0x40000
	s_addc_u32 s59, s47, 0
	global_load_dwordx4 v[42:45], v195, s[58:59]
	s_add_u32 s58, s46, 0x60000
	s_addc_u32 s59, s47, 0
	global_load_dwordx4 v[46:49], v195, s[58:59]
	s_add_u32 s58, s46, 0x80000
	s_addc_u32 s59, s47, 0
	global_load_dwordx4 v[50:53], v195, s[58:59]
	s_add_u32 s58, s46, 0xa0000
	s_addc_u32 s59, s47, 0
	global_load_dwordx4 v[54:57], v195, s[58:59]
	s_add_u32 s58, s46, 0xc0000
	s_addc_u32 s59, s47, 0
	global_load_dwordx4 v[58:61], v195, s[58:59]
	s_add_u32 s46, s46, 0xe0000
	s_addc_u32 s47, s47, 0
	global_load_dwordx4 v[62:65], v195, s[46:47]
	s_mov_b64 s[46:47], 0

.LBB0_978:
	ds_read_b128 v[176:179], v162
	v_lshl_add_u64 v[180:181], v[164:165], 0, s[22:23]
	s_waitcnt lgkmcnt(0)
	global_store_dwordx4 v[180:181], v[176:179], off
	s_add_i32 s98, s98, 1
	s_or_b64 exec, exec, s[44:45]
	s_and_saveexec_b64 s[44:45], s[12:13]
	s_cbranch_execz .LBB0_974
.LBB0_979:
	ds_read_b128 v[176:179], v199
	v_lshl_add_u64 v[180:181], v[166:167], 0, s[22:23]
	s_waitcnt lgkmcnt(0)
	global_store_dwordx4 v[180:181], v[176:179], off
	s_add_i32 s98, s98, 1
	s_or_b64 exec, exec, s[44:45]
	s_and_saveexec_b64 s[44:45], s[14:15]
	s_cbranch_execz .LBB0_975
.LBB0_980:
	ds_read_b128 v[176:179], v200
	v_lshl_add_u64 v[180:181], v[168:169], 0, s[22:23]
	s_waitcnt lgkmcnt(0)
	global_store_dwordx4 v[180:181], v[176:179], off
	s_add_i32 s98, s98, 1
	s_or_b64 exec, exec, s[44:45]
	s_and_saveexec_b64 s[44:45], s[16:17]
	s_cbranch_execz .LBB0_976
.LBB0_981:
	ds_read_b128 v[176:179], v201
	v_lshl_add_u64 v[180:181], v[170:171], 0, s[22:23]
	s_waitcnt lgkmcnt(0)
	global_store_dwordx4 v[180:181], v[176:179], off
	s_add_i32 s98, s98, 1
	s_or_b64 exec, exec, s[44:45]
	s_and_saveexec_b64 s[44:45], s[18:19]
	s_cbranch_execz .LBB0_977
.LBB0_982:
	ds_read_b128 v[176:179], v202
	v_lshl_add_u64 v[180:181], v[172:173], 0, s[22:23]
	s_waitcnt lgkmcnt(0)
	global_store_dwordx4 v[180:181], v[176:179], off
	s_add_i32 s98, s98, 1
	s_or_b64 exec, exec, s[44:45]
	s_and_saveexec_b64 s[44:45], s[20:21]
	s_cbranch_execz .LBB0_966

.LBB0_989:
	v_bfe_u32 v139, v131, 4, 2
	s_lshl_b32 s13, s12, 1
	s_waitcnt lgkmcnt(0)
	s_barrier
	v_lshlrev_b32_e32 v140, 10, v139
	v_lshlrev_b32_e32 v137, 7, v137
	s_cmp_ge_i32 s13, s49
	v_add3_u32 v137, 0, v140, v137
	v_lshlrev_b32_e32 v140, 1, v139
	s_cselect_b64 s[20:21], -1, 0
	v_bfe_u32 v141, v131, 3, 1
	v_and_or_b32 v140, v140, 2, v141
	s_cmp_lg_u64 s[28:29], 0
	s_cselect_b64 s[38:39], -1, 0
	s_lshl_b32 s12, s12, 12
	s_add_i32 s12, s12, 0
	v_lshlrev_b32_e32 v140, 5, v140
	s_add_i32 s12, s12, 0x10000
	v_and_b32_e32 v157, 7, v131
	v_bitop3_b32 v131, v138, v131, 7 bitop3:0x78
	v_add3_u32 v156, v137, v135, v140
	v_lshlrev_b32_e32 v133, 7, v133
	v_lshlrev_b32_e32 v135, 2, v139
	v_lshl_add_u32 v142, v131, 4, s12
	v_or_b32_e32 v131, 8, v138
	v_add3_u32 v158, s12, v133, v135
	v_or_b32_e32 v133, s16, v131
	v_lshlrev_b32_e32 v144, 7, v131
	v_or_b32_e32 v131, 16, v138
	v_cmp_gt_i32_e64 s[12:13], s48, v133
	v_or_b32_e32 v133, s16, v131
	v_cmp_gt_i32_e64 s[14:15], s48, v133
	v_lshlrev_b32_e32 v145, 7, v131
	s_waitcnt vmcnt(1)
	v_ashrrev_i32_e32 v133, 31, v132
	v_or_b32_e32 v131, 24, v138
	v_ashrrev_i32_e32 v137, 31, v136
	v_ashrrev_i32_e32 v135, 31, v134
	v_lshlrev_b64 v[140:141], 10, v[132:133]
	v_or_b32_e32 v132, s16, v131
	v_lshlrev_b32_e32 v146, 7, v131
	s_waitcnt vmcnt(0)
	v_ashrrev_i32_e32 v131, 31, v130
	v_lshlrev_b32_e32 v143, 7, v138
	v_lshlrev_b64 v[136:137], 10, v[136:137]
	v_lshlrev_b64 v[134:135], 10, v[134:135]
	v_lshlrev_b64 v[138:139], 10, v[130:131]
	v_lshlrev_b32_e32 v162, 4, v157
	v_cmp_gt_i32_e64 s[16:17], s48, v132
	v_lshl_add_u64 v[130:131], s[26:27], 0, v[136:137]
	v_lshl_add_u64 v[132:133], s[26:27], 0, v[134:135]
	v_lshl_add_u64 v[134:135], s[26:27], 0, v[140:141]
	v_lshl_add_u64 v[136:137], s[26:27], 0, v[138:139]
	v_lshl_add_u64 v[130:131], v[130:131], 0, v[162:163]
	v_lshl_add_u64 v[132:133], v[132:133], 0, v[162:163]
	v_lshl_add_u64 v[134:135], v[134:135], 0, v[162:163]
	v_lshl_add_u64 v[136:137], v[136:137], 0, v[162:163]
	s_mov_b32 s44, 0
	v_add_u32_e32 v159, v142, v143
	v_add_u32_e32 v160, v142, v144
	v_add_u32_e32 v161, v142, v145
	v_add_u32_e32 v162, v142, v146
	s_mov_b32 s40, 0
	s_mov_b32 s98, 0
	s_branch .LBB0_992

.Lmy_yd_992:
	s_mov_b32 s98, 0
	s_and_b32 s22, s40, 1
	s_lshl_b32 s46, s22, 15
	s_cmp_gt_u32 s40, 13
	s_cselect_b64 s[42:43], -1, 0
	s_and_b64 s[42:43], s[38:39], s[42:43]
	v_sub_co_u32_e64 v138, s[40:41], s40, 14
	s_and_b64 s[52:53], s[38:39], exec
	v_readfirstlane_b32 s45, v138
	s_cselect_b32 s47, s45, 15
	s_add_i32 s45, s45, 16
	s_and_b64 s[40:41], s[40:41], exec
	s_cselect_b32 s40, s45, s47
	s_and_b64 s[42:43], s[42:43], exec
	s_cselect_b32 s47, s29, s19
	s_cselect_b32 s52, s28, s18
	s_mov_b64 s[42:43], -1
	s_andn2_b64 vcc, exec, s[20:21]
	v_subrev_u32_e32 v164, s46, v154
	v_cvt_pk_bf16_f32 v152, v34, v35
	v_cvt_pk_bf16_f32 v153, v36, v37
	v_cvt_pk_bf16_f32 v150, v38, v39
	v_cvt_pk_bf16_f32 v151, v40, v41
	v_cvt_pk_bf16_f32 v148, v42, v43
	v_cvt_pk_bf16_f32 v149, v44, v45
	v_cvt_pk_bf16_f32 v146, v46, v47
	v_cvt_pk_bf16_f32 v147, v48, v49
	v_cvt_pk_bf16_f32 v144, v50, v51
	v_cvt_pk_bf16_f32 v145, v52, v53
	v_cvt_pk_bf16_f32 v142, v54, v55
	v_cvt_pk_bf16_f32 v143, v56, v57
	v_cvt_pk_bf16_f32 v140, v58, v59
	v_cvt_pk_bf16_f32 v141, v60, v61
	v_cvt_pk_bf16_f32 v138, v62, v63
	v_cvt_pk_bf16_f32 v139, v64, v65
	s_cbranch_vccnz .LBB0_994
	s_ashr_i32 s41, s40, 31
	s_lshl_b64 s[42:43], s[40:41], 8
	s_add_u32 s42, s52, s42
	s_addc_u32 s43, s47, s43
	ds_write2st64_b64 v164, v[152:153], v[150:151] offset0:64 offset1:72
	ds_write2st64_b64 v164, v[148:149], v[146:147] offset0:80 offset1:88
	ds_write2st64_b64 v164, v[144:145], v[142:143] offset0:96 offset1:104
	ds_write2st64_b64 v164, v[140:141], v[138:139] offset0:112 offset1:120
	s_add_u32 s54, s42, 0x20000
	global_load_dwordx4 v[34:37], v155, s[42:43]
	s_addc_u32 s55, s43, 0
	global_load_dwordx4 v[38:41], v155, s[54:55]
	s_add_u32 s54, s42, 0x40000
	s_addc_u32 s55, s43, 0
	global_load_dwordx4 v[42:45], v155, s[54:55]
	s_add_u32 s54, s42, 0x60000
	s_addc_u32 s55, s43, 0
	global_load_dwordx4 v[46:49], v155, s[54:55]
	s_add_u32 s54, s42, 0x80000
	s_addc_u32 s55, s43, 0
	global_load_dwordx4 v[50:53], v155, s[54:55]
	s_add_u32 s54, s42, 0xa0000
	s_addc_u32 s55, s43, 0
	global_load_dwordx4 v[54:57], v155, s[54:55]
	s_add_u32 s54, s42, 0xc0000
	s_addc_u32 s55, s43, 0
	global_load_dwordx4 v[58:61], v155, s[54:55]
	s_add_u32 s42, s42, 0xe0000
	s_addc_u32 s43, s43, 0
	global_load_dwordx4 v[62:65], v155, s[42:43]
	s_mov_b64 s[42:43], 0

.LBB0_1000:
	ds_read_b128 v[138:141], v159
	v_lshl_add_u64 v[142:143], v[130:131], 0, s[22:23]
	s_waitcnt lgkmcnt(0)
	global_store_dwordx4 v[142:143], v[138:141], off
	s_add_i32 s98, s98, 1
	s_or_b64 exec, exec, s[40:41]
	s_and_saveexec_b64 s[40:41], s[12:13]
	s_cbranch_execz .LBB0_998
.LBB0_1001:
	ds_read_b128 v[138:141], v160
	v_lshl_add_u64 v[142:143], v[132:133], 0, s[22:23]
	s_waitcnt lgkmcnt(0)
	global_store_dwordx4 v[142:143], v[138:141], off
	s_add_i32 s98, s98, 1
	s_or_b64 exec, exec, s[40:41]
	s_and_saveexec_b64 s[40:41], s[14:15]
	s_cbranch_execz .LBB0_999
.LBB0_1002:
	ds_read_b128 v[138:141], v161
	v_lshl_add_u64 v[142:143], v[134:135], 0, s[22:23]
	s_waitcnt lgkmcnt(0)
	global_store_dwordx4 v[142:143], v[138:141], off
	s_add_i32 s98, s98, 1
	s_or_b64 exec, exec, s[40:41]
	s_and_saveexec_b64 s[40:41], s[16:17]
	s_cbranch_execz .LBB0_990

.LBB0_1009:
	v_bfe_u32 v73, v67, 4, 2
	s_waitcnt lgkmcnt(0)
	s_barrier
	v_lshlrev_b32_e32 v74, 10, v73
	v_lshlrev_b32_e32 v72, 7, v72
	s_cmp_ge_i32 s13, s49
	v_add3_u32 v72, 0, v74, v72
	v_lshlrev_b32_e32 v74, 1, v73
	s_cselect_b64 s[16:17], -1, 0
	v_bfe_u32 v75, v67, 3, 1
	v_and_or_b32 v74, v74, 2, v75
	s_cmp_lg_u64 s[28:29], 0
	s_cselect_b64 s[18:19], -1, 0
	s_lshl_b32 s13, s13, 11
	s_add_i32 s13, s13, 0
	v_lshlrev_b32_e32 v74, 5, v74
	s_add_i32 s13, s13, 0x10000
	v_and_b32_e32 v89, 7, v67
	v_bitop3_b32 v67, v70, v67, 7 bitop3:0x78
	v_add3_u32 v88, v72, v71, v74
	v_lshlrev_b32_e32 v69, 7, v69
	v_lshlrev_b32_e32 v71, 2, v73
	v_lshl_add_u32 v72, v67, 4, s13
	v_or_b32_e32 v67, 8, v70
	v_add3_u32 v90, s13, v69, v71
	v_lshlrev_b32_e32 v73, 7, v70
	s_waitcnt vmcnt(1)
	v_ashrrev_i32_e32 v69, 31, v68
	v_or_b32_e32 v70, s12, v67
	v_lshlrev_b32_e32 v74, 7, v67
	s_waitcnt vmcnt(0)
	v_ashrrev_i32_e32 v67, 31, v66
	v_lshlrev_b64 v[68:69], 10, v[68:69]
	v_cmp_gt_i32_e64 s[12:13], s48, v70
	v_lshlrev_b64 v[70:71], 10, v[66:67]
	v_lshlrev_b32_e32 v162, 4, v89
	v_lshl_add_u64 v[66:67], s[26:27], 0, v[68:69]
	v_lshl_add_u64 v[68:69], s[26:27], 0, v[70:71]
	v_lshl_add_u64 v[66:67], v[66:67], 0, v[162:163]
	v_lshl_add_u64 v[68:69], v[68:69], 0, v[162:163]
	s_mov_b32 s34, 0
	v_add_u32_e32 v91, v72, v73
	v_add_u32_e32 v92, v72, v74
	s_mov_b32 s20, 0
	s_mov_b32 s98, 0
	s_branch .LBB0_1012
